# v10 + nt cache policy on prologue streaming loads (ada weights, dense weight conversion sources)
# speedup vs baseline: 1.0413x; 1.0061x over previous
; #define LAS __attribute__((address_space(3)))
; __device__ __forceinline__ void ada_phase(LAS float* sm, int bid, int G, const float* c, const float* ada_w, const float* ada_b, float* ada) {
;     ...
;     for (int j = bid; j < 192; j += G) {
;         const int l = j / 96, cb = j - l * 96;
;         const float* w = ada_w + (size_t)l * D * 12288 + (size_t)(kg * 128) * 12288 + cb * 128 + c4 * 4;
;         float4 a = make_float4(0.f, 0.f, 0.f, 0.f);
; #pragma unroll 8
;         for (int k = 0; k < 128; ++k) { const float4 wv = *(const float4*)(w + (size_t)k * 12288); const float s = cs[kg * 128 + k]; a.x += s * wv.x; a.y += s * wv.y; a.z += s * wv.z; a.w += s * wv.w; }
;         __syncthreads();
;         LAS float* rp = red + kg * 128 + c4 * 4; rp[0] = a.x; rp[1] = a.y; rp[2] = a.z; rp[3] = a.w;
;         __syncthreads();
;         if (tid < 128) { float s = 0.f;
; #pragma unroll
;             for (int q = 0; q < 16; ++q) s += red[q * 128 + tid];
;             ada[l * 12288 + cb * 128 + tid] = s + ada_b[l * 12288 + cb * 128 + tid]; }
;     }
.LBB0_23:
	v_lshl_add_u64 v[42:43], v[10:11], 0, s[4:5]
	v_add_co_u32_e32 v18, vcc, s8, v42
	global_load_dwordx4 v[14:17], v[42:43], off nt
	s_nop 0
	v_addc_co_u32_e32 v19, vcc, 0, v43, vcc
	v_add_co_u32_e32 v30, vcc, s11, v42
	global_load_dwordx4 v[18:21], v[18:19], off nt
	s_nop 0
	v_addc_co_u32_e32 v31, vcc, 0, v43, vcc
	v_add_co_u32_e32 v32, vcc, s12, v42
	s_add_u32 s4, s4, 0x60000
	s_nop 0
	v_addc_co_u32_e32 v33, vcc, 0, v43, vcc
	v_add_co_u32_e32 v38, vcc, s13, v42
	global_load_dwordx4 v[22:25], v[30:31], off nt
	global_load_dwordx4 v[26:29], v[32:33], off nt
	v_addc_co_u32_e32 v39, vcc, 0, v43, vcc
	v_add_co_u32_e32 v40, vcc, s14, v42
	s_addc_u32 s5, s5, 0
	s_nop 0
	v_addc_co_u32_e32 v41, vcc, 0, v43, vcc
	v_add_co_u32_e32 v44, vcc, s15, v42
	global_load_dwordx4 v[30:33], v[38:39], off nt
	global_load_dwordx4 v[34:37], v[40:41], off nt
	v_addc_co_u32_e32 v45, vcc, 0, v43, vcc
	v_add_co_u32_e32 v42, vcc, s16, v42
	global_load_dwordx4 v[38:41], v[44:45], off nt
	s_nop 0
	v_addc_co_u32_e32 v43, vcc, 0, v43, vcc
	global_load_dwordx4 v[42:45], v[42:43], off nt
	ds_read_b128 v[46:49], v13
	ds_read_b128 v[50:53], v13 offset:16
	v_add_u32_e32 v13, 32, v13
	s_cmp_eq_u32 s4, 0x600000
	s_waitcnt lgkmcnt(1)
	v_mov_b32_e32 v54, v49
	s_waitcnt lgkmcnt(0)
	v_mov_b32_e32 v56, v53
	s_waitcnt vmcnt(7)
	v_pk_fma_f32 v[2:3], v[14:15], v[46:47], v[2:3] op_sel_hi:[1,0,1]
	v_pk_fma_f32 v[4:5], v[16:17], v[46:47], v[4:5] op_sel_hi:[1,0,1]
	s_waitcnt vmcnt(6)
	v_pk_fma_f32 v[2:3], v[18:19], v[46:47], v[2:3] op_sel:[0,1,0]
	v_pk_fma_f32 v[4:5], v[20:21], v[46:47], v[4:5] op_sel:[0,1,0]
	s_waitcnt vmcnt(5)
	v_pk_fma_f32 v[2:3], v[22:23], v[48:49], v[2:3] op_sel_hi:[1,0,1]
	v_pk_fma_f32 v[4:5], v[24:25], v[48:49], v[4:5] op_sel_hi:[1,0,1]
	s_waitcnt vmcnt(4)
	v_pk_fma_f32 v[2:3], v[26:27], v[54:55], v[2:3] op_sel_hi:[1,0,1]
	v_pk_fma_f32 v[4:5], v[28:29], v[54:55], v[4:5] op_sel_hi:[1,0,1]
	s_waitcnt vmcnt(3)
	v_pk_fma_f32 v[2:3], v[30:31], v[50:51], v[2:3] op_sel_hi:[1,0,1]
	v_pk_fma_f32 v[4:5], v[32:33], v[50:51], v[4:5] op_sel_hi:[1,0,1]
	s_waitcnt vmcnt(2)
	v_pk_fma_f32 v[2:3], v[34:35], v[50:51], v[2:3] op_sel:[0,1,0]
	v_pk_fma_f32 v[4:5], v[36:37], v[50:51], v[4:5] op_sel:[0,1,0]
	s_waitcnt vmcnt(1)
	v_pk_fma_f32 v[2:3], v[38:39], v[52:53], v[2:3] op_sel_hi:[1,0,1]
	v_pk_fma_f32 v[4:5], v[40:41], v[52:53], v[4:5] op_sel_hi:[1,0,1]
	s_waitcnt vmcnt(0)
	v_pk_fma_f32 v[2:3], v[42:43], v[56:57], v[2:3] op_sel_hi:[1,0,1]
	v_pk_fma_f32 v[4:5], v[44:45], v[56:57], v[4:5] op_sel_hi:[1,0,1]
	s_cbranch_scc0 .LBB0_23
	s_barrier
	ds_write_b128 v7, v[2:5] offset:8192
	s_waitcnt lgkmcnt(0)
	s_barrier
	s_and_saveexec_b64 s[4:5], s[0:1]
	s_cbranch_execz .LBB0_21
	s_mulk_i32 s19, 0xffa0
	s_add_i32 s19, s19, s17
	s_lshl_b32 s19, s19, 7
	s_add_i32 s19, s19, s18
	v_add_u32_e32 v2, s19, v6
	v_ashrrev_i32_e32 v3, 31, v2
	v_lshlrev_b64 v[2:3], 2, v[2:3]
	v_lshl_add_u64 v[4:5], s[6:7], 0, v[2:3]
	global_load_dword v13, v[4:5], off
	ds_read2st64_b32 v[4:5], v12 offset0:32 offset1:34
	ds_read2st64_b32 v[10:11], v12 offset0:36 offset1:38
	ds_read2st64_b32 v[14:15], v12 offset0:40 offset1:42
	ds_read2st64_b32 v[16:17], v12 offset0:44 offset1:46
	ds_read2st64_b32 v[18:19], v12 offset0:48 offset1:50
	ds_read2st64_b32 v[20:21], v12 offset0:52 offset1:54
	ds_read2st64_b32 v[22:23], v12 offset0:56 offset1:58
	ds_read2st64_b32 v[24:25], v12 offset0:60 offset1:62
	s_waitcnt lgkmcnt(7)
	v_add_f32_e32 v4, 0, v4
	v_add_f32_e32 v4, v4, v5
	s_waitcnt lgkmcnt(6)
	v_add_f32_e32 v4, v4, v10
	v_add_f32_e32 v4, v4, v11
	s_waitcnt lgkmcnt(5)
	v_add_f32_e32 v4, v4, v14
	v_add_f32_e32 v4, v4, v15
	s_waitcnt lgkmcnt(4)
	v_add_f32_e32 v4, v4, v16
	v_add_f32_e32 v4, v4, v17
	s_waitcnt lgkmcnt(3)
	v_add_f32_e32 v4, v4, v18
	v_add_f32_e32 v4, v4, v19
	s_waitcnt lgkmcnt(2)
	v_add_f32_e32 v4, v4, v20
	v_add_f32_e32 v4, v4, v21
	s_waitcnt lgkmcnt(1)
	v_add_f32_e32 v4, v4, v22
	v_add_f32_e32 v4, v4, v23
	s_waitcnt lgkmcnt(0)
	v_add_f32_e32 v4, v4, v24
	v_add_f32_e32 v4, v4, v25
	v_lshl_add_u64 v[2:3], s[2:3], 0, v[2:3]
	s_waitcnt vmcnt(0)
	v_add_f32_e32 v4, v4, v13
	global_store_dword v[2:3], v4, off
	s_branch .LBB0_21

; __device__ __forceinline__ int tid_fresh() { int t = threadIdx.x; asm volatile("" : "+v"(t)); return t; }
; #define CVT_LOAD(jx) do { const int b_ = (jx) / per, r_ = (jx) - b_ * per, kt_ = r_ / tn, nt_ = r_ - kt_ * tn; \
;         const float* s_ = src + (size_t)b_ * sbs + (size_t)(kt_ * 64) * ldS + nt_ * 256; \
;         _Pragma("unroll") for (int q = 0; q < 8; ++q) v[q] = *(const float4*)(s_ + (size_t)(kr + 8 * q) * ldS + c4 * 4); } while (0)
;     const int tid = tid_fresh();
;     const int tk = K / 64, tn = N / 256, per = tk * tn, total = per * nbatch;
;     const int kr = tid >> 6, c4 = tid & 63;
;     ...
;     float4 v[8];
;     if (bid < total) CVT_LOAD(bid);
.LBB0_91:
	s_or_b64 exec, exec, s[8:9]
	s_cmpk_lt_i32 s42, 0x300
	s_mul_hi_i32 s0, s42, 0x2aaaaaab
	s_cselect_b64 s[2:3], -1, 0
	s_lshr_b32 s1, s0, 31
	s_lshr_b32 s0, s0, 7
	s_add_i32 s0, s0, s1
	s_mulk_i32 s0, 0x300
	s_sub_i32 s0, s42, s0
	s_mul_i32 s1, s0, 0x2aab
	s_lshr_b32 s4, s1, 31
	s_ashr_i32 s13, s1, 18
	s_add_i32 s13, s13, s4
	s_mul_i32 s1, s13, 0xffffffe8
	s_add_i32 s1, s1, s0
	s_lshl_b32 s0, s1, 8
	s_ashr_i32 s1, s0, 31
	v_readlane_b32 s8, v254, 0
	s_mov_b32 s14, s42
	s_cmpk_gt_i32 s42, 0x2ff
	v_readlane_b32 s9, v254, 1
	v_mov_b32_e32 v59, v0
	s_barrier
	s_cbranch_scc1 .LBB0_97
	s_load_dwordx2 s[4:5], s[8:9], 0x30
	s_load_dwordx2 s[6:7], s[8:9], 0x118
	s_mul_i32 s8, s13, 0x60000
	s_ashr_i32 s9, s8, 31
	s_lshl_b64 s[8:9], s[8:9], 2
	s_waitcnt lgkmcnt(0)
	s_add_u32 s10, s4, s8
	s_addc_u32 s11, s5, s9
	s_lshl_b64 s[8:9], s[0:1], 2
	v_and_b32_e32 v1, 63, v59
	s_add_u32 s8, s10, s8
	v_ashrrev_i32_e32 v56, 6, v59
	s_addc_u32 s9, s11, s9
	v_mov_b32_e32 v35, 0
	v_lshlrev_b32_e32 v34, 4, v1
	s_movk_i32 s10, 0x1800
	v_lshl_add_u64 v[26:27], s[8:9], 0, v[34:35]
	v_mad_i64_i32 v[36:37], s[8:9], v56, s10, 0
	v_add_u32_e32 v2, 8, v56
	v_lshl_add_u64 v[10:11], v[36:37], 2, v[26:27]
	v_mad_i64_i32 v[38:39], s[8:9], v2, s10, 0
	v_lshl_add_u64 v[12:13], v[38:39], 2, v[26:27]
	global_load_dwordx4 v[2:5], v[10:11], off nt
	global_load_dwordx4 v[6:9], v[12:13], off nt
	v_add_u32_e32 v10, 16, v56
	v_mad_i64_i32 v[40:41], s[8:9], v10, s10, 0
	v_add_u32_e32 v10, 24, v56
	v_lshl_add_u64 v[18:19], v[40:41], 2, v[26:27]
	v_mad_i64_i32 v[42:43], s[8:9], v10, s10, 0
	v_lshl_add_u64 v[20:21], v[42:43], 2, v[26:27]
	global_load_dwordx4 v[10:13], v[18:19], off nt
	global_load_dwordx4 v[14:17], v[20:21], off nt
	v_add_u32_e32 v18, 32, v56
	v_mad_i64_i32 v[44:45], s[8:9], v18, s10, 0
	v_add_u32_e32 v18, 40, v56
	v_lshl_add_u64 v[28:29], v[44:45], 2, v[26:27]
	v_mad_i64_i32 v[46:47], s[8:9], v18, s10, 0
	v_lshl_add_u64 v[30:31], v[46:47], 2, v[26:27]
	global_load_dwordx4 v[18:21], v[28:29], off nt
	global_load_dwordx4 v[22:25], v[30:31], off nt
	v_add_u32_e32 v28, 48, v56
	v_mad_i64_i32 v[48:49], s[8:9], v28, s10, 0
	v_add_u32_e32 v28, 56, v56
	v_lshl_add_u64 v[52:53], v[48:49], 2, v[26:27]
	v_mad_i64_i32 v[50:51], s[8:9], v28, s10, 0
	v_lshl_add_u64 v[54:55], v[50:51], 2, v[26:27]
	global_load_dwordx4 v[26:29], v[52:53], off nt
	global_load_dwordx4 v[30:33], v[54:55], off nt
	v_lshlrev_b32_e32 v62, 2, v1
	v_and_b32_e32 v1, 7, v59
	v_add_u32_e32 v61, 0, v34
	v_lshlrev_b32_e32 v34, 4, v1
	s_movk_i32 s8, 0x2020
	v_lshl_add_u64 v[52:53], s[6:7], 0, v[34:35]
	s_mov_b64 s[6:7], 0x30000
	v_mad_u32_u24 v60, v1, s8, 0
	v_lshl_add_u64 v[52:53], v[52:53], 0, s[6:7]
	s_movk_i32 s6, 0x404
	v_ashrrev_i32_e32 v1, 3, v59
	v_add_u32_e32 v55, 0x200, v59
	v_add_u32_e32 v57, 0x400, v59
	v_add_u32_e32 v59, 0x600, v59
	v_mul_lo_u32 v34, v56, s6
	v_ashrrev_i32_e32 v55, 3, v55
	v_ashrrev_i32_e32 v57, 3, v57
	v_ashrrev_i32_e32 v59, 3, v59
	v_lshl_add_u32 v54, v1, 2, v60
	v_lshl_add_u32 v56, v55, 2, v60
	v_lshl_add_u32 v58, v57, 2, v60
	v_lshl_add_u32 v60, v59, 2, v60
	v_add_u32_e32 v61, v61, v34
	v_lshlrev_b32_e32 v34, 2, v62
	s_mov_b32 s9, s14
	s_branch .LBB0_94

; #define LAS __attribute__((address_space(3)))
; #define CVT_LOAD(jx) do { const int b_ = (jx) / per, r_ = (jx) - b_ * per, kt_ = r_ / tn, nt_ = r_ - kt_ * tn; \
;         const float* s_ = src + (size_t)b_ * sbs + (size_t)(kt_ * 64) * ldS + nt_ * 256; \
;         _Pragma("unroll") for (int q = 0; q < 8; ++q) v[q] = *(const float4*)(s_ + (size_t)(kr + 8 * q) * ldS + c4 * 4); } while (0)
;     ...
;     for (int j = bid; j < total; j += G) {
;         const int b = j / per, r = j - b * per, kt = r / tn, ntile = r - kt * tn;
;         __syncthreads();
; #pragma unroll
;         for (int q = 0; q < 8; ++q) { LAS float* tp = tile + (kr + 8 * q) * 257 + c4 * 4; tp[0] = v[q].x; tp[1] = v[q].y; tp[2] = v[q].z; tp[3] = v[q].w; }
;         if (j + G < total) CVT_LOAD(j + G);
;         __syncthreads();
.LBB0_94:
	s_nop 0
	v_add_u32_e32 v62, 0x2020, v61
	s_barrier
	s_waitcnt vmcnt(7)
	ds_write2_b32 v61, v2, v3 offset1:1
	ds_write2_b32 v61, v4, v5 offset0:2 offset1:3
	s_waitcnt vmcnt(6)
	ds_write2_b32 v62, v6, v7 offset1:1
	v_add_u32_e32 v62, 0x2028, v61
	ds_write2_b32 v62, v8, v9 offset1:1
	v_add_u32_e32 v62, 0x4040, v61
	s_waitcnt vmcnt(5)
	ds_write2_b32 v62, v10, v11 offset1:1
	v_add_u32_e32 v62, 0x4048, v61
	ds_write2_b32 v62, v12, v13 offset1:1
	v_add_u32_e32 v62, 0x6060, v61
	s_waitcnt vmcnt(4)
	ds_write2_b32 v62, v14, v15 offset1:1
	v_add_u32_e32 v62, 0x6068, v61
	ds_write2_b32 v62, v16, v17 offset1:1
	v_add_u32_e32 v62, 0x8080, v61
	s_waitcnt vmcnt(3)
	ds_write2_b32 v62, v18, v19 offset1:1
	v_add_u32_e32 v62, 0x8088, v61
	ds_write2_b32 v62, v20, v21 offset1:1
	v_add_u32_e32 v62, 0xa0a0, v61
	s_waitcnt vmcnt(2)
	ds_write2_b32 v62, v22, v23 offset1:1
	v_add_u32_e32 v62, 0xa0a8, v61
	v_readlane_b32 s6, v254, 4
	ds_write2_b32 v62, v24, v25 offset1:1
	v_add_u32_e32 v62, 0xc0c0, v61
	s_add_i32 s8, s9, s6
	s_waitcnt vmcnt(1)
	ds_write2_b32 v62, v26, v27 offset1:1
	v_add_u32_e32 v62, 0xc0c8, v61
	s_cmpk_gt_i32 s8, 0x2ff
	ds_write2_b32 v62, v28, v29 offset1:1
	v_add_u32_e32 v62, 0xe0e0, v61
	s_cselect_b64 s[6:7], -1, 0
	s_waitcnt vmcnt(0)
	ds_write2_b32 v62, v30, v31 offset1:1
	v_add_u32_e32 v62, 0xe0e8, v61
	s_and_b64 vcc, exec, s[6:7]
	ds_write2_b32 v62, v32, v33 offset1:1
	s_cbranch_vccnz .LBB0_93
	s_mul_hi_i32 s10, s8, 0x2aaaaaab
	s_lshr_b32 s11, s10, 31
	s_lshr_b32 s10, s10, 7
	s_add_i32 s10, s10, s11
	s_mulk_i32 s10, 0x300
	s_sub_i32 s10, s8, s10
	s_mul_i32 s11, s10, 0x2aab
	s_lshr_b32 s14, s11, 31
	s_ashr_i32 s11, s11, 18
	s_add_i32 s11, s11, s14
	s_mul_i32 s14, s11, 0xffffffe8
	s_add_i32 s14, s14, s10
	s_mul_i32 s10, s11, 0x60000
	s_ashr_i32 s11, s10, 31
	s_lshl_b64 s[10:11], s[10:11], 2
	s_add_u32 s15, s4, s10
	s_addc_u32 s17, s5, s11
	s_lshl_b32 s10, s14, 8
	s_ashr_i32 s11, s10, 31
	s_lshl_b64 s[10:11], s[10:11], 2
	s_add_u32 s10, s15, s10
	s_addc_u32 s11, s17, s11
	v_lshl_add_u64 v[26:27], s[10:11], 0, v[34:35]
	v_lshl_add_u64 v[10:11], v[36:37], 2, v[26:27]
	v_lshl_add_u64 v[12:13], v[38:39], 2, v[26:27]
	v_lshl_add_u64 v[18:19], v[40:41], 2, v[26:27]
	v_lshl_add_u64 v[20:21], v[42:43], 2, v[26:27]
	v_lshl_add_u64 v[28:29], v[44:45], 2, v[26:27]
	v_lshl_add_u64 v[30:31], v[46:47], 2, v[26:27]
	v_lshl_add_u64 v[62:63], v[48:49], 2, v[26:27]
	global_load_dwordx4 v[2:5], v[10:11], off nt
	global_load_dwordx4 v[6:9], v[12:13], off nt
	s_nop 0
	global_load_dwordx4 v[10:13], v[18:19], off nt
	global_load_dwordx4 v[14:17], v[20:21], off nt
	s_nop 0
	global_load_dwordx4 v[18:21], v[28:29], off nt
	global_load_dwordx4 v[22:25], v[30:31], off nt
	v_lshl_add_u64 v[64:65], v[50:51], 2, v[26:27]
	global_load_dwordx4 v[26:29], v[62:63], off nt
	global_load_dwordx4 v[30:33], v[64:65], off nt
	s_branch .LBB0_93

; __device__ __forceinline__ int tid_fresh() { int t = threadIdx.x; asm volatile("" : "+v"(t)); return t; }
; #define CVT_LOAD(jx) do { const int b_ = (jx) / per, r_ = (jx) - b_ * per, kt_ = r_ / tn, nt_ = r_ - kt_ * tn; \
;         const float* s_ = src + (size_t)b_ * sbs + (size_t)(kt_ * 64) * ldS + nt_ * 256; \
;         _Pragma("unroll") for (int q = 0; q < 8; ++q) v[q] = *(const float4*)(s_ + (size_t)(kr + 8 * q) * ldS + c4 * 4); } while (0)
;     const int tid = tid_fresh();
;     const int tk = K / 64, tn = N / 256, per = tk * tn, total = per * nbatch;
;     const int kr = tid >> 6, c4 = tid & 63;
;     ...
;     float4 v[8];
;     if (bid < total) CVT_LOAD(bid);
.LBB0_97:
	s_cmpk_lt_i32 s14, 0x100
	s_cselect_b64 s[4:5], -1, 0
	s_ashr_i32 s15, s14, 31
	s_lshr_b32 s6, s15, 24
	s_add_i32 s6, s14, s6
	s_and_b32 s6, s6, 0xffffff00
	s_sub_i32 s8, s14, s6
	s_bfe_u32 s6, s8, 0x3001c
	s_add_i32 s6, s8, s6
	s_sext_i32_i16 s6, s6
	s_ashr_i32 s9, s6, 3
	s_lshl_b32 s6, s9, 6
	s_lshl_b32 s9, s9, 11
	s_lshl_b32 s8, s8, 8
	v_writelane_b32 v254, s14, 19
	s_ashr_i32 s7, s6, 31
	s_sub_i32 s8, s8, s9
	v_writelane_b32 v254, s15, 20
	s_lshl_b64 s[6:7], s[6:7], 13
	s_ashr_i32 s9, s8, 31
	v_readlane_b32 s18, v254, 0
	s_cmpk_gt_i32 s14, 0xff
	v_readlane_b32 s19, v254, 1
	v_mov_b32_e32 v59, v0
	s_barrier
	s_cbranch_scc1 .LBB0_102
	s_load_dwordx2 s[10:11], s[18:19], 0x90
	s_load_dwordx2 s[14:15], s[18:19], 0x118
	v_and_b32_e32 v1, 63, v59
	v_ashrrev_i32_e32 v54, 6, v59
	v_mov_b32_e32 v35, 0
	s_waitcnt lgkmcnt(0)
	s_add_u32 s17, s10, s6
	s_addc_u32 s20, s11, s7
	s_lshl_b64 s[18:19], s[8:9], 2
	s_add_u32 s18, s17, s18
	s_addc_u32 s19, s20, s19
	v_lshlrev_b32_e32 v34, 4, v1
	v_ashrrev_i32_e32 v55, 31, v54
	v_add_u32_e32 v38, 8, v54
	s_waitcnt vmcnt(5)
	v_lshl_add_u64 v[26:27], s[18:19], 0, v[34:35]
	v_lshlrev_b64 v[2:3], 13, v[54:55]
	v_ashrrev_i32_e32 v39, 31, v38
	v_add_u32_e32 v40, 16, v54
	v_lshl_add_u64 v[10:11], v[26:27], 0, v[2:3]
	v_lshlrev_b64 v[2:3], 13, v[38:39]
	v_ashrrev_i32_e32 v41, 31, v40
	v_add_u32_e32 v42, 24, v54
	v_lshl_add_u64 v[12:13], v[26:27], 0, v[2:3]
	global_load_dwordx4 v[2:5], v[10:11], off nt
	global_load_dwordx4 v[6:9], v[12:13], off nt
	v_lshlrev_b64 v[10:11], 13, v[40:41]
	v_ashrrev_i32_e32 v43, 31, v42
	v_add_u32_e32 v44, 32, v54
	v_lshl_add_u64 v[18:19], v[26:27], 0, v[10:11]
	v_lshlrev_b64 v[10:11], 13, v[42:43]
	v_ashrrev_i32_e32 v45, 31, v44
	v_add_u32_e32 v46, 40, v54
	v_lshl_add_u64 v[20:21], v[26:27], 0, v[10:11]
	global_load_dwordx4 v[10:13], v[18:19], off nt
	global_load_dwordx4 v[14:17], v[20:21], off nt
	v_lshlrev_b64 v[18:19], 13, v[44:45]
	v_ashrrev_i32_e32 v47, 31, v46
	v_add_u32_e32 v48, 48, v54
	v_lshl_add_u64 v[28:29], v[26:27], 0, v[18:19]
	v_lshlrev_b64 v[18:19], 13, v[46:47]
	v_ashrrev_i32_e32 v49, 31, v48
	v_add_u32_e32 v50, 56, v54
	s_waitcnt vmcnt(8)
	v_lshl_add_u64 v[30:31], v[26:27], 0, v[18:19]
	global_load_dwordx4 v[18:21], v[28:29], off nt
	global_load_dwordx4 v[22:25], v[30:31], off nt
	v_lshlrev_b64 v[28:29], 13, v[48:49]
	v_ashrrev_i32_e32 v51, 31, v50
	v_lshl_add_u64 v[36:37], v[26:27], 0, v[28:29]
	v_lshlrev_b64 v[28:29], 13, v[50:51]
	v_lshl_add_u64 v[52:53], v[26:27], 0, v[28:29]
	global_load_dwordx4 v[26:29], v[36:37], off nt
	global_load_dwordx4 v[30:33], v[52:53], off nt
	v_lshlrev_b32_e32 v62, 2, v1
	v_and_b32_e32 v1, 7, v59
	v_add_u32_e32 v61, 0, v34
	v_lshlrev_b32_e32 v34, 4, v1
	s_movk_i32 s17, 0x2020
	v_lshl_add_u64 v[52:53], s[14:15], 0, v[34:35]
	s_mov_b64 s[14:15], 0x1830000
	v_lshlrev_b64 v[36:37], 11, v[54:55]
	v_mad_u32_u24 v60, v1, s17, 0
	v_lshl_add_u64 v[52:53], v[52:53], 0, s[14:15]
	s_movk_i32 s14, 0x404
	v_ashrrev_i32_e32 v1, 3, v59
	v_add_u32_e32 v55, 0x200, v59
	v_add_u32_e32 v57, 0x400, v59
	v_add_u32_e32 v59, 0x600, v59
	v_mul_lo_u32 v34, v54, s14
	v_ashrrev_i32_e32 v55, 3, v55
	v_ashrrev_i32_e32 v57, 3, v57
	v_ashrrev_i32_e32 v59, 3, v59
	v_readlane_b32 s14, v254, 19
	v_lshlrev_b64 v[38:39], 11, v[38:39]
	v_lshlrev_b64 v[40:41], 11, v[40:41]
	v_lshlrev_b64 v[42:43], 11, v[42:43]
	v_lshlrev_b64 v[44:45], 11, v[44:45]
	v_lshlrev_b64 v[46:47], 11, v[46:47]
	v_lshlrev_b64 v[48:49], 11, v[48:49]
	v_lshlrev_b64 v[50:51], 11, v[50:51]
	v_lshl_add_u32 v54, v1, 2, v60
	v_lshl_add_u32 v56, v55, 2, v60
	v_lshl_add_u32 v58, v57, 2, v60
	v_lshl_add_u32 v60, v59, 2, v60
	v_add_u32_e32 v61, v61, v34
	v_lshlrev_b32_e32 v34, 2, v62
	s_mov_b32 s18, s14
	v_readlane_b32 s15, v254, 20
	s_branch .LBB0_100

; #define LAS __attribute__((address_space(3)))
; __device__ __forceinline__ int tid_fresh() { int t = threadIdx.x; asm volatile("" : "+v"(t)); return t; }
; #define CVT_LOAD(jx) do { const int b_ = (jx) / per, r_ = (jx) - b_ * per, kt_ = r_ / tn, nt_ = r_ - kt_ * tn; \
;         const float* s_ = src + (size_t)b_ * sbs + (size_t)(kt_ * 64) * ldS + nt_ * 256; \
;         _Pragma("unroll") for (int q = 0; q < 8; ++q) v[q] = *(const float4*)(s_ + (size_t)(kr + 8 * q) * ldS + c4 * 4); } while (0)
;     const int tid = tid_fresh();
;     const int tk = K / 64, tn = N / 256, per = tk * tn, total = per * nbatch;
;     const int kr = tid >> 6, c4 = tid & 63;
;     ...
;     float4 v[8];
;     if (bid < total) CVT_LOAD(bid);
;     for (int j = bid; j < total; j += G) {
;         const int b = j / per, r = j - b * per, kt = r / tn, ntile = r - kt * tn;
;         __syncthreads();
; #pragma unroll
;         for (int q = 0; q < 8; ++q) { LAS float* tp = tile + (kr + 8 * q) * 257 + c4 * 4; tp[0] = v[q].x; tp[1] = v[q].y; tp[2] = v[q].z; tp[3] = v[q].w; }
;         if (j + G < total) CVT_LOAD(j + G);
;         __syncthreads();
.LBB0_100:
	s_nop 0
	v_add_u32_e32 v62, 0x2020, v61
	s_barrier
	s_waitcnt vmcnt(7)
	ds_write2_b32 v61, v2, v3 offset1:1
	ds_write2_b32 v61, v4, v5 offset0:2 offset1:3
	s_waitcnt vmcnt(6)
	ds_write2_b32 v62, v6, v7 offset1:1
	v_add_u32_e32 v62, 0x2028, v61
	ds_write2_b32 v62, v8, v9 offset1:1
	v_add_u32_e32 v62, 0x4040, v61
	s_waitcnt vmcnt(5)
	ds_write2_b32 v62, v10, v11 offset1:1
	v_add_u32_e32 v62, 0x4048, v61
	ds_write2_b32 v62, v12, v13 offset1:1
	v_add_u32_e32 v62, 0x6060, v61
	s_waitcnt vmcnt(4)
	ds_write2_b32 v62, v14, v15 offset1:1
	v_add_u32_e32 v62, 0x6068, v61
	ds_write2_b32 v62, v16, v17 offset1:1
	v_add_u32_e32 v62, 0x8080, v61
	s_waitcnt vmcnt(3)
	ds_write2_b32 v62, v18, v19 offset1:1
	v_add_u32_e32 v62, 0x8088, v61
	ds_write2_b32 v62, v20, v21 offset1:1
	v_add_u32_e32 v62, 0xa0a0, v61
	s_waitcnt vmcnt(2)
	ds_write2_b32 v62, v22, v23 offset1:1
	v_add_u32_e32 v62, 0xa0a8, v61
	v_readlane_b32 s14, v254, 4
	ds_write2_b32 v62, v24, v25 offset1:1
	v_add_u32_e32 v62, 0xc0c0, v61
	s_add_i32 s17, s18, s14
	s_waitcnt vmcnt(1)
	ds_write2_b32 v62, v26, v27 offset1:1
	v_add_u32_e32 v62, 0xc0c8, v61
	s_cmpk_gt_i32 s17, 0xff
	ds_write2_b32 v62, v28, v29 offset1:1
	v_add_u32_e32 v62, 0xe0e0, v61
	s_cselect_b64 s[14:15], -1, 0
	s_waitcnt vmcnt(0)
	ds_write2_b32 v62, v30, v31 offset1:1
	v_add_u32_e32 v62, 0xe0e8, v61
	s_and_b64 vcc, exec, s[14:15]
	ds_write2_b32 v62, v32, v33 offset1:1
	s_cbranch_vccnz .LBB0_99
	s_ashr_i32 s19, s17, 31
	s_lshr_b32 s19, s19, 24
	s_add_i32 s19, s17, s19
	s_and_b32 s19, s19, 0xffffff00
	s_sub_i32 s19, s17, s19
	s_bfe_u32 s20, s19, 0x3001c
	s_add_i32 s20, s19, s20
	s_sext_i32_i16 s20, s20
	s_ashr_i32 s22, s20, 3
	s_lshl_b32 s20, s22, 6
	s_ashr_i32 s21, s20, 31
	s_lshl_b64 s[20:21], s[20:21], 13
	s_add_u32 s23, s10, s20
	s_addc_u32 s24, s11, s21
	s_lshl_b32 s20, s22, 11
	s_lshl_b32 s19, s19, 8
	s_sub_i32 s20, s19, s20
	s_ashr_i32 s21, s20, 31
	s_lshl_b64 s[20:21], s[20:21], 2
	s_add_u32 s20, s23, s20
	s_addc_u32 s21, s24, s21
	v_lshl_add_u64 v[26:27], s[20:21], 0, v[34:35]
	v_lshl_add_u64 v[10:11], v[36:37], 2, v[26:27]
	v_lshl_add_u64 v[12:13], v[38:39], 2, v[26:27]
	v_lshl_add_u64 v[18:19], v[40:41], 2, v[26:27]
	v_lshl_add_u64 v[20:21], v[42:43], 2, v[26:27]
	v_lshl_add_u64 v[28:29], v[44:45], 2, v[26:27]
	v_lshl_add_u64 v[30:31], v[46:47], 2, v[26:27]
	v_lshl_add_u64 v[62:63], v[48:49], 2, v[26:27]
	global_load_dwordx4 v[2:5], v[10:11], off nt
	global_load_dwordx4 v[6:9], v[12:13], off nt
	s_nop 0
	global_load_dwordx4 v[10:13], v[18:19], off nt
	global_load_dwordx4 v[14:17], v[20:21], off nt
	s_nop 0
	global_load_dwordx4 v[18:21], v[28:29], off nt
	global_load_dwordx4 v[22:25], v[30:31], off nt
	v_lshl_add_u64 v[64:65], v[50:51], 2, v[26:27]
	global_load_dwordx4 v[26:29], v[62:63], off nt
	global_load_dwordx4 v[30:33], v[64:65], off nt
	s_branch .LBB0_99
.LBB0_102:
	v_readlane_b32 s14, v254, 0
	v_readlane_b32 s15, v254, 1
	v_mov_b32_e32 v59, v0
	s_andn2_b64 vcc, exec, s[2:3]
	s_barrier
	s_cbranch_vccnz .LBB0_107
	s_load_dwordx2 s[2:3], s[14:15], 0x98
	s_load_dwordx2 s[10:11], s[14:15], 0x118
	s_mul_i32 s14, s13, 0x60800
	s_ashr_i32 s15, s14, 31
	s_lshl_b64 s[14:15], s[14:15], 2
	s_waitcnt lgkmcnt(0)
	s_add_u32 s13, s2, s14
	s_addc_u32 s14, s3, s15
	s_lshl_b64 s[0:1], s[0:1], 2
	v_and_b32_e32 v1, 63, v59
	s_add_u32 s0, s13, s0
	v_ashrrev_i32_e32 v56, 6, v59
	s_addc_u32 s1, s14, s1
	v_mov_b32_e32 v35, 0
	v_lshlrev_b32_e32 v34, 4, v1
	s_movk_i32 s13, 0x1820
	s_waitcnt vmcnt(5)
	v_lshl_add_u64 v[26:27], s[0:1], 0, v[34:35]
	v_mad_i64_i32 v[36:37], s[0:1], v56, s13, 0
	v_add_u32_e32 v2, 8, v56
	v_lshl_add_u64 v[10:11], v[36:37], 2, v[26:27]
	v_mad_i64_i32 v[38:39], s[0:1], v2, s13, 0
	v_lshl_add_u64 v[12:13], v[38:39], 2, v[26:27]
	global_load_dwordx4 v[2:5], v[10:11], off nt
	global_load_dwordx4 v[6:9], v[12:13], off nt
	v_add_u32_e32 v10, 16, v56
	v_mad_i64_i32 v[40:41], s[0:1], v10, s13, 0
	v_add_u32_e32 v10, 24, v56
	v_lshl_add_u64 v[18:19], v[40:41], 2, v[26:27]
	v_mad_i64_i32 v[42:43], s[0:1], v10, s13, 0
	v_lshl_add_u64 v[20:21], v[42:43], 2, v[26:27]
	global_load_dwordx4 v[10:13], v[18:19], off nt
	global_load_dwordx4 v[14:17], v[20:21], off nt
	v_add_u32_e32 v18, 32, v56
	v_mad_i64_i32 v[44:45], s[0:1], v18, s13, 0
	v_add_u32_e32 v18, 40, v56
	v_lshl_add_u64 v[28:29], v[44:45], 2, v[26:27]
	v_mad_i64_i32 v[46:47], s[0:1], v18, s13, 0
	s_waitcnt vmcnt(8)
	v_lshl_add_u64 v[30:31], v[46:47], 2, v[26:27]
	global_load_dwordx4 v[18:21], v[28:29], off nt
	global_load_dwordx4 v[22:25], v[30:31], off nt
	v_add_u32_e32 v28, 48, v56
	v_mad_i64_i32 v[48:49], s[0:1], v28, s13, 0
	v_add_u32_e32 v28, 56, v56
	v_lshl_add_u64 v[52:53], v[48:49], 2, v[26:27]
	v_mad_i64_i32 v[50:51], s[0:1], v28, s13, 0
	v_lshl_add_u64 v[54:55], v[50:51], 2, v[26:27]
	global_load_dwordx4 v[26:29], v[52:53], off nt
	global_load_dwordx4 v[30:33], v[54:55], off nt
	v_lshlrev_b32_e32 v62, 2, v1
	v_and_b32_e32 v1, 7, v59
	v_add_u32_e32 v61, 0, v34
	s_movk_i32 s0, 0x2020
	v_lshlrev_b32_e32 v34, 4, v1
	v_mad_u32_u24 v60, v1, s0, 0
	v_lshl_add_u64 v[52:53], s[10:11], 0, v[34:35]
	s_mov_b64 s[0:1], 0x2030000
	v_lshl_add_u64 v[52:53], v[52:53], 0, s[0:1]
	s_movk_i32 s0, 0x404
	v_ashrrev_i32_e32 v1, 3, v59
	v_add_u32_e32 v55, 0x200, v59
	v_add_u32_e32 v57, 0x400, v59
	v_add_u32_e32 v59, 0x600, v59
	v_mul_lo_u32 v34, v56, s0
	v_ashrrev_i32_e32 v55, 3, v55
	v_ashrrev_i32_e32 v57, 3, v57
	v_ashrrev_i32_e32 v59, 3, v59
	v_readlane_b32 s0, v254, 19
	v_lshl_add_u32 v54, v1, 2, v60
	v_lshl_add_u32 v56, v55, 2, v60
	v_lshl_add_u32 v58, v57, 2, v60
	v_lshl_add_u32 v60, v59, 2, v60
	v_add_u32_e32 v61, v61, v34
	v_lshlrev_b32_e32 v34, 2, v62
	s_mov_b32 s11, s0
	v_readlane_b32 s1, v254, 20
	s_branch .LBB0_105

; #define LAS __attribute__((address_space(3)))
; __device__ __forceinline__ int tid_fresh() { int t = threadIdx.x; asm volatile("" : "+v"(t)); return t; }
; #define CVT_LOAD(jx) do { const int b_ = (jx) / per, r_ = (jx) - b_ * per, kt_ = r_ / tn, nt_ = r_ - kt_ * tn; \
;         const float* s_ = src + (size_t)b_ * sbs + (size_t)(kt_ * 64) * ldS + nt_ * 256; \
;         _Pragma("unroll") for (int q = 0; q < 8; ++q) v[q] = *(const float4*)(s_ + (size_t)(kr + 8 * q) * ldS + c4 * 4); } while (0)
;     const int tid = tid_fresh();
;     const int tk = K / 64, tn = N / 256, per = tk * tn, total = per * nbatch;
;     const int kr = tid >> 6, c4 = tid & 63;
;     ...
;     float4 v[8];
;     if (bid < total) CVT_LOAD(bid);
;     for (int j = bid; j < total; j += G) {
;         const int b = j / per, r = j - b * per, kt = r / tn, ntile = r - kt * tn;
;         __syncthreads();
; #pragma unroll
;         for (int q = 0; q < 8; ++q) { LAS float* tp = tile + (kr + 8 * q) * 257 + c4 * 4; tp[0] = v[q].x; tp[1] = v[q].y; tp[2] = v[q].z; tp[3] = v[q].w; }
;         if (j + G < total) CVT_LOAD(j + G);
;         __syncthreads();
.LBB0_105:
	s_nop 0
	v_add_u32_e32 v62, 0x2020, v61
	s_barrier
	s_waitcnt vmcnt(7)
	ds_write2_b32 v61, v2, v3 offset1:1
	ds_write2_b32 v61, v4, v5 offset0:2 offset1:3
	s_waitcnt vmcnt(6)
	ds_write2_b32 v62, v6, v7 offset1:1
	v_add_u32_e32 v62, 0x2028, v61
	ds_write2_b32 v62, v8, v9 offset1:1
	v_add_u32_e32 v62, 0x4040, v61
	s_waitcnt vmcnt(5)
	ds_write2_b32 v62, v10, v11 offset1:1
	v_add_u32_e32 v62, 0x4048, v61
	ds_write2_b32 v62, v12, v13 offset1:1
	v_add_u32_e32 v62, 0x6060, v61
	s_waitcnt vmcnt(4)
	ds_write2_b32 v62, v14, v15 offset1:1
	v_add_u32_e32 v62, 0x6068, v61
	ds_write2_b32 v62, v16, v17 offset1:1
	v_add_u32_e32 v62, 0x8080, v61
	s_waitcnt vmcnt(3)
	ds_write2_b32 v62, v18, v19 offset1:1
	v_add_u32_e32 v62, 0x8088, v61
	ds_write2_b32 v62, v20, v21 offset1:1
	v_add_u32_e32 v62, 0xa0a0, v61
	s_waitcnt vmcnt(2)
	ds_write2_b32 v62, v22, v23 offset1:1
	v_add_u32_e32 v62, 0xa0a8, v61
	v_readlane_b32 s0, v254, 4
	ds_write2_b32 v62, v24, v25 offset1:1
	v_add_u32_e32 v62, 0xc0c0, v61
	s_add_i32 s10, s11, s0
	s_waitcnt vmcnt(1)
	ds_write2_b32 v62, v26, v27 offset1:1
	v_add_u32_e32 v62, 0xc0c8, v61
	s_cmpk_gt_i32 s10, 0x2ff
	ds_write2_b32 v62, v28, v29 offset1:1
	v_add_u32_e32 v62, 0xe0e0, v61
	s_cselect_b64 s[0:1], -1, 0
	s_waitcnt vmcnt(0)
	ds_write2_b32 v62, v30, v31 offset1:1
	v_add_u32_e32 v62, 0xe0e8, v61
	s_and_b64 vcc, exec, s[0:1]
	ds_write2_b32 v62, v32, v33 offset1:1
	s_cbranch_vccnz .LBB0_104
	s_mul_hi_i32 s13, s10, 0x2aaaaaab
	s_lshr_b32 s14, s13, 31
	s_lshr_b32 s13, s13, 7
	s_add_i32 s13, s13, s14
	s_mulk_i32 s13, 0x300
	s_sub_i32 s13, s10, s13
	s_mul_i32 s14, s13, 0x2aab
	s_lshr_b32 s15, s14, 31
	s_ashr_i32 s14, s14, 18
	s_add_i32 s14, s14, s15
	s_mul_i32 s15, s14, 0xffffffe8
	s_mul_i32 s14, s14, 0x60800
	s_add_i32 s13, s15, s13
	s_ashr_i32 s15, s14, 31
	s_lshl_b64 s[14:15], s[14:15], 2
	s_add_u32 s17, s2, s14
	s_addc_u32 s18, s3, s15
	s_lshl_b32 s14, s13, 8
	s_ashr_i32 s15, s14, 31
	s_lshl_b64 s[14:15], s[14:15], 2
	s_add_u32 s14, s17, s14
	s_addc_u32 s15, s18, s15
	v_lshl_add_u64 v[26:27], s[14:15], 0, v[34:35]
	v_lshl_add_u64 v[10:11], v[36:37], 2, v[26:27]
	v_lshl_add_u64 v[12:13], v[38:39], 2, v[26:27]
	v_lshl_add_u64 v[18:19], v[40:41], 2, v[26:27]
	v_lshl_add_u64 v[20:21], v[42:43], 2, v[26:27]
	v_lshl_add_u64 v[28:29], v[44:45], 2, v[26:27]
	v_lshl_add_u64 v[30:31], v[46:47], 2, v[26:27]
	v_lshl_add_u64 v[62:63], v[48:49], 2, v[26:27]
	global_load_dwordx4 v[2:5], v[10:11], off nt
	global_load_dwordx4 v[6:9], v[12:13], off nt
	s_nop 0
	global_load_dwordx4 v[10:13], v[18:19], off nt
	global_load_dwordx4 v[14:17], v[20:21], off nt
	s_nop 0
	global_load_dwordx4 v[18:21], v[28:29], off nt
	global_load_dwordx4 v[22:25], v[30:31], off nt
	v_lshl_add_u64 v[64:65], v[50:51], 2, v[26:27]
	global_load_dwordx4 v[26:29], v[62:63], off nt
	global_load_dwordx4 v[30:33], v[64:65], off nt
	s_branch .LBB0_104
.LBB0_107:
	v_cndmask_b32_e64 v1, 0, 1, s[4:5]
	v_cmp_ne_u32_e64 s[0:1], 1, v1
	v_readlane_b32 s10, v254, 0
	v_readlane_b32 s11, v254, 1
	v_writelane_b32 v255, s0, 26
	v_mov_b32_e32 v59, v0
	s_andn2_b64 vcc, exec, s[4:5]
	v_writelane_b32 v255, s1, 27
	s_barrier
	s_cbranch_vccnz .LBB0_112
	s_load_dwordx2 s[0:1], s[10:11], 0xc0
	s_load_dwordx2 s[2:3], s[10:11], 0x118
	v_and_b32_e32 v1, 63, v59
	v_ashrrev_i32_e32 v54, 6, v59
	v_mov_b32_e32 v35, 0
	s_waitcnt lgkmcnt(0)
	s_add_u32 s6, s0, s6
	s_addc_u32 s7, s1, s7
	s_lshl_b64 s[4:5], s[8:9], 2
	s_add_u32 s4, s6, s4
	s_addc_u32 s5, s7, s5
	v_lshlrev_b32_e32 v34, 4, v1
	v_ashrrev_i32_e32 v55, 31, v54
	v_add_u32_e32 v38, 8, v54
	s_waitcnt vmcnt(5)
	v_lshl_add_u64 v[26:27], s[4:5], 0, v[34:35]
	v_lshlrev_b64 v[2:3], 13, v[54:55]
	v_ashrrev_i32_e32 v39, 31, v38
	v_add_u32_e32 v40, 16, v54
	v_lshl_add_u64 v[10:11], v[26:27], 0, v[2:3]
	v_lshlrev_b64 v[2:3], 13, v[38:39]
	v_ashrrev_i32_e32 v41, 31, v40
	v_add_u32_e32 v42, 24, v54
	v_lshl_add_u64 v[12:13], v[26:27], 0, v[2:3]
	global_load_dwordx4 v[2:5], v[10:11], off nt
	global_load_dwordx4 v[6:9], v[12:13], off nt
	v_lshlrev_b64 v[10:11], 13, v[40:41]
	v_ashrrev_i32_e32 v43, 31, v42
	v_add_u32_e32 v44, 32, v54
	v_lshl_add_u64 v[18:19], v[26:27], 0, v[10:11]
	v_lshlrev_b64 v[10:11], 13, v[42:43]
	v_ashrrev_i32_e32 v45, 31, v44
	v_add_u32_e32 v46, 40, v54
	v_lshl_add_u64 v[20:21], v[26:27], 0, v[10:11]
	global_load_dwordx4 v[10:13], v[18:19], off nt
	global_load_dwordx4 v[14:17], v[20:21], off nt
	v_lshlrev_b64 v[18:19], 13, v[44:45]
	v_ashrrev_i32_e32 v47, 31, v46
	v_add_u32_e32 v48, 48, v54
	v_lshl_add_u64 v[28:29], v[26:27], 0, v[18:19]
	v_lshlrev_b64 v[18:19], 13, v[46:47]
	v_ashrrev_i32_e32 v49, 31, v48
	v_add_u32_e32 v50, 56, v54
	s_waitcnt vmcnt(8)
	v_lshl_add_u64 v[30:31], v[26:27], 0, v[18:19]
	global_load_dwordx4 v[18:21], v[28:29], off nt
	global_load_dwordx4 v[22:25], v[30:31], off nt
	v_lshlrev_b64 v[28:29], 13, v[48:49]
	v_ashrrev_i32_e32 v51, 31, v50
	v_lshl_add_u64 v[36:37], v[26:27], 0, v[28:29]
	v_lshlrev_b64 v[28:29], 13, v[50:51]
	v_lshl_add_u64 v[52:53], v[26:27], 0, v[28:29]
	global_load_dwordx4 v[26:29], v[36:37], off nt
	global_load_dwordx4 v[30:33], v[52:53], off nt
	v_lshlrev_b32_e32 v62, 2, v1
	v_and_b32_e32 v1, 7, v59
	v_add_u32_e32 v61, 0, v34
	v_lshlrev_b32_e32 v34, 4, v1
	s_movk_i32 s4, 0x2020
	v_lshl_add_u64 v[52:53], s[2:3], 0, v[34:35]
	s_mov_b64 s[2:3], 0x3830000
	v_lshlrev_b64 v[36:37], 11, v[54:55]
	v_mad_u32_u24 v60, v1, s4, 0
	v_lshl_add_u64 v[52:53], v[52:53], 0, s[2:3]
	s_movk_i32 s2, 0x404
	v_ashrrev_i32_e32 v1, 3, v59
	v_add_u32_e32 v55, 0x200, v59
	v_add_u32_e32 v57, 0x400, v59
	v_add_u32_e32 v59, 0x600, v59
	v_mul_lo_u32 v34, v54, s2
	v_ashrrev_i32_e32 v55, 3, v55
	v_ashrrev_i32_e32 v57, 3, v57
	v_ashrrev_i32_e32 v59, 3, v59
	v_readlane_b32 s2, v254, 19
	v_lshlrev_b64 v[38:39], 11, v[38:39]
	v_lshlrev_b64 v[40:41], 11, v[40:41]
	v_lshlrev_b64 v[42:43], 11, v[42:43]
	v_lshlrev_b64 v[44:45], 11, v[44:45]
	v_lshlrev_b64 v[46:47], 11, v[46:47]
	v_lshlrev_b64 v[48:49], 11, v[48:49]
	v_lshlrev_b64 v[50:51], 11, v[50:51]
	v_lshl_add_u32 v54, v1, 2, v60
	v_lshl_add_u32 v56, v55, 2, v60
	v_lshl_add_u32 v58, v57, 2, v60
	v_lshl_add_u32 v60, v59, 2, v60
	v_add_u32_e32 v61, v61, v34
	v_lshlrev_b32_e32 v34, 2, v62
	s_mov_b32 s5, s2
	v_readlane_b32 s3, v254, 20
	s_branch .LBB0_110

; #define LAS __attribute__((address_space(3)))
; #define CVT_LOAD(jx) do { const int b_ = (jx) / per, r_ = (jx) - b_ * per, kt_ = r_ / tn, nt_ = r_ - kt_ * tn; \
;         const float* s_ = src + (size_t)b_ * sbs + (size_t)(kt_ * 64) * ldS + nt_ * 256; \
;         _Pragma("unroll") for (int q = 0; q < 8; ++q) v[q] = *(const float4*)(s_ + (size_t)(kr + 8 * q) * ldS + c4 * 4); } while (0)
;     ...
;     for (int j = bid; j < total; j += G) {
;         const int b = j / per, r = j - b * per, kt = r / tn, ntile = r - kt * tn;
;         __syncthreads();
; #pragma unroll
;         for (int q = 0; q < 8; ++q) { LAS float* tp = tile + (kr + 8 * q) * 257 + c4 * 4; tp[0] = v[q].x; tp[1] = v[q].y; tp[2] = v[q].z; tp[3] = v[q].w; }
;         if (j + G < total) CVT_LOAD(j + G);
;         __syncthreads();
.LBB0_110:
	s_nop 0
	v_add_u32_e32 v62, 0x2020, v61
	s_barrier
	s_waitcnt vmcnt(7)
	ds_write2_b32 v61, v2, v3 offset1:1
	ds_write2_b32 v61, v4, v5 offset0:2 offset1:3
	s_waitcnt vmcnt(6)
	ds_write2_b32 v62, v6, v7 offset1:1
	v_add_u32_e32 v62, 0x2028, v61
	ds_write2_b32 v62, v8, v9 offset1:1
	v_add_u32_e32 v62, 0x4040, v61
	s_waitcnt vmcnt(5)
	ds_write2_b32 v62, v10, v11 offset1:1
	v_add_u32_e32 v62, 0x4048, v61
	ds_write2_b32 v62, v12, v13 offset1:1
	v_add_u32_e32 v62, 0x6060, v61
	s_waitcnt vmcnt(4)
	ds_write2_b32 v62, v14, v15 offset1:1
	v_add_u32_e32 v62, 0x6068, v61
	ds_write2_b32 v62, v16, v17 offset1:1
	v_add_u32_e32 v62, 0x8080, v61
	s_waitcnt vmcnt(3)
	ds_write2_b32 v62, v18, v19 offset1:1
	v_add_u32_e32 v62, 0x8088, v61
	ds_write2_b32 v62, v20, v21 offset1:1
	v_add_u32_e32 v62, 0xa0a0, v61
	s_waitcnt vmcnt(2)
	ds_write2_b32 v62, v22, v23 offset1:1
	v_add_u32_e32 v62, 0xa0a8, v61
	v_readlane_b32 s2, v254, 4
	ds_write2_b32 v62, v24, v25 offset1:1
	v_add_u32_e32 v62, 0xc0c0, v61
	s_add_i32 s4, s5, s2
	s_waitcnt vmcnt(1)
	ds_write2_b32 v62, v26, v27 offset1:1
	v_add_u32_e32 v62, 0xc0c8, v61
	s_cmpk_gt_i32 s4, 0xff
	ds_write2_b32 v62, v28, v29 offset1:1
	v_add_u32_e32 v62, 0xe0e0, v61
	s_cselect_b64 s[2:3], -1, 0
	s_waitcnt vmcnt(0)
	ds_write2_b32 v62, v30, v31 offset1:1
	v_add_u32_e32 v62, 0xe0e8, v61
	s_and_b64 vcc, exec, s[2:3]
	ds_write2_b32 v62, v32, v33 offset1:1
	s_cbranch_vccnz .LBB0_109
	s_ashr_i32 s6, s4, 31
	s_lshr_b32 s6, s6, 24
	s_add_i32 s6, s4, s6
	s_and_b32 s6, s6, 0xffffff00
	s_sub_i32 s8, s4, s6
	s_bfe_u32 s6, s8, 0x3001c
	s_add_i32 s6, s8, s6
	s_sext_i32_i16 s6, s6
	s_ashr_i32 s9, s6, 3
	s_lshl_b32 s6, s9, 6
	s_ashr_i32 s7, s6, 31
	s_lshl_b64 s[6:7], s[6:7], 13
	s_add_u32 s10, s0, s6
	s_addc_u32 s11, s1, s7
	s_lshl_b32 s6, s9, 11
	s_lshl_b32 s7, s8, 8
	s_sub_i32 s6, s7, s6
	s_ashr_i32 s7, s6, 31
	s_lshl_b64 s[6:7], s[6:7], 2
	s_add_u32 s6, s10, s6
	s_addc_u32 s7, s11, s7
	v_lshl_add_u64 v[26:27], s[6:7], 0, v[34:35]
	v_lshl_add_u64 v[10:11], v[36:37], 2, v[26:27]
	v_lshl_add_u64 v[12:13], v[38:39], 2, v[26:27]
	v_lshl_add_u64 v[18:19], v[40:41], 2, v[26:27]
	v_lshl_add_u64 v[20:21], v[42:43], 2, v[26:27]
	v_lshl_add_u64 v[28:29], v[44:45], 2, v[26:27]
	v_lshl_add_u64 v[30:31], v[46:47], 2, v[26:27]
	v_lshl_add_u64 v[62:63], v[48:49], 2, v[26:27]
	global_load_dwordx4 v[2:5], v[10:11], off nt
	global_load_dwordx4 v[6:9], v[12:13], off nt
	s_nop 0
	global_load_dwordx4 v[10:13], v[18:19], off nt
	global_load_dwordx4 v[14:17], v[20:21], off nt
	s_nop 0
	global_load_dwordx4 v[18:21], v[28:29], off nt
	global_load_dwordx4 v[22:25], v[30:31], off nt
	v_lshl_add_u64 v[64:65], v[50:51], 2, v[26:27]
	global_load_dwordx4 v[26:29], v[62:63], off nt
	global_load_dwordx4 v[30:33], v[64:65], off nt
	s_branch .LBB0_109

; __device__ __forceinline__ int tid_fresh() { int t = threadIdx.x; asm volatile("" : "+v"(t)); return t; }
; __device__ __forceinline__ KP kparams() { KP q = (KP)__builtin_amdgcn_kernarg_segment_ptr(); asm volatile("" : "+s"(q)); return q; }
; #define CVT_LOAD(jx) do { const int b_ = (jx) / per, r_ = (jx) - b_ * per, kt_ = r_ / tn, nt_ = r_ - kt_ * tn; \
;         const float* s_ = src + (size_t)b_ * sbs + (size_t)(kt_ * 64) * ldS + nt_ * 256; \
;         _Pragma("unroll") for (int q = 0; q < 8; ++q) v[q] = *(const float4*)(s_ + (size_t)(kr + 8 * q) * ldS + c4 * 4); } while (0)
;     const int tid = tid_fresh();
;     const int tk = K / 64, tn = N / 256, per = tk * tn, total = per * nbatch;
;     const int kr = tid >> 6, c4 = tid & 63;
;     ...
;     float4 v[8];
;     if (bid < total) CVT_LOAD(bid);
; __global__ void __launch_bounds__(NTHR, 2) fwd(Params p_unused) {
;     ...
; #pragma unroll 1
;         for (int l2 = 0; l2 < 2 * REP_CVT; ++l2) { const int l = l2 & 1;
;             KP kp = kparams(); bf16_t* Wgu = (bf16_t*)(kp->ws + WS_WGU) + l * WGU_L; bf16_t* Wd = (bf16_t*)(kp->ws + WS_WD) + l * WD_L;
;             cvt_group(tile, bid, G, kp->in[30] + (size_t)l * D * FF, 0, FF, D, FF, Wgu + (size_t)NE * 1024 * D, 0, 1, 1, 1024);
;             cvt_group(tile, bid, G, kp->in[31] + (size_t)l * D * FF, 0, FF, D, FF, Wgu + (size_t)NE * 1024 * D, 0, 2, 1, 1024);
.LBB0_114:
	v_readlane_b32 s18, v254, 0
	v_readlane_b32 s19, v254, 1
	s_load_dwordx2 s[20:21], s[18:19], 0x118
	s_mul_i32 s22, s14, 0x10400000
	v_mov_b32_e32 v61, v0
	s_waitcnt lgkmcnt(0)
	s_add_u32 s27, s20, s22
	s_addc_u32 s28, s21, 0
	s_lshl_b64 s[22:23], s[14:15], 20
	s_add_u32 s20, s27, 0x14030000
	s_addc_u32 s21, s28, 0
	s_and_b64 vcc, exec, s[0:1]
	s_cbranch_vccnz .LBB0_119
	s_load_dwordx2 s[24:25], s[18:19], 0xf0
	s_lshl_b64 s[30:31], s[22:23], 2
	v_and_b32_e32 v1, 63, v61
	v_ashrrev_i32_e32 v52, 6, v61
	v_lshlrev_b32_e32 v34, 4, v1
	s_waitcnt lgkmcnt(0)
	s_add_u32 s29, s24, s30
	s_addc_u32 s30, s25, s31
	s_add_u32 s24, s29, s2
	s_addc_u32 s25, s30, s3
	s_add_u32 s24, s24, s6
	s_addc_u32 s25, s25, s7
	v_ashrrev_i32_e32 v53, 31, v52
	v_add_u32_e32 v38, 8, v52
	s_waitcnt vmcnt(5)
	v_lshl_add_u64 v[26:27], s[24:25], 0, v[34:35]
	v_lshlrev_b64 v[2:3], 11, v[52:53]
	v_ashrrev_i32_e32 v39, 31, v38
	v_add_u32_e32 v40, 16, v52
	v_lshl_add_u64 v[10:11], v[26:27], 0, v[2:3]
	v_lshlrev_b64 v[2:3], 11, v[38:39]
	v_ashrrev_i32_e32 v41, 31, v40
	v_add_u32_e32 v42, 24, v52
	v_lshl_add_u64 v[12:13], v[26:27], 0, v[2:3]
	global_load_dwordx4 v[2:5], v[10:11], off nt
	global_load_dwordx4 v[6:9], v[12:13], off nt
	v_lshlrev_b64 v[10:11], 11, v[40:41]
	v_ashrrev_i32_e32 v43, 31, v42
	v_add_u32_e32 v44, 32, v52
	v_lshl_add_u64 v[18:19], v[26:27], 0, v[10:11]
	v_lshlrev_b64 v[10:11], 11, v[42:43]
	v_ashrrev_i32_e32 v45, 31, v44
	v_add_u32_e32 v46, 40, v52
	v_lshl_add_u64 v[20:21], v[26:27], 0, v[10:11]
	global_load_dwordx4 v[10:13], v[18:19], off nt
	global_load_dwordx4 v[14:17], v[20:21], off nt
	v_lshlrev_b64 v[18:19], 11, v[44:45]
	v_ashrrev_i32_e32 v47, 31, v46
	v_add_u32_e32 v48, 48, v52
	v_lshl_add_u64 v[28:29], v[26:27], 0, v[18:19]
	v_lshlrev_b64 v[18:19], 11, v[46:47]
	v_ashrrev_i32_e32 v49, 31, v48
	v_add_u32_e32 v50, 56, v52
	s_waitcnt vmcnt(8)
	v_lshl_add_u64 v[30:31], v[26:27], 0, v[18:19]
	global_load_dwordx4 v[18:21], v[28:29], off nt
	global_load_dwordx4 v[22:25], v[30:31], off nt
	v_lshlrev_b64 v[28:29], 11, v[48:49]
	v_ashrrev_i32_e32 v51, 31, v50
	v_lshl_add_u64 v[36:37], v[26:27], 0, v[28:29]
	v_lshlrev_b64 v[28:29], 11, v[50:51]
	v_lshl_add_u64 v[54:55], v[26:27], 0, v[28:29]
	global_load_dwordx4 v[26:29], v[36:37], off nt
	global_load_dwordx4 v[30:33], v[54:55], off nt
	v_lshlrev_b32_e32 v66, 2, v1
	v_lshlrev_b64 v[36:37], 9, v[52:53]
	v_and_b32_e32 v1, 7, v61
	v_mul_lo_u32 v64, v52, s17
	v_ashrrev_i32_e32 v52, 3, v61
	v_add_u32_e32 v55, 0x200, v61
	v_add_u32_e32 v58, 0x400, v61
	v_add_u32_e32 v61, 0x600, v61
	v_add_u32_e32 v34, 0, v34
	v_mad_u32_u24 v63, v1, s13, 0
	v_ashrrev_i32_e32 v55, 3, v55
	v_ashrrev_i32_e32 v58, 3, v58
	v_ashrrev_i32_e32 v61, 3, v61
	v_readlane_b32 s24, v254, 19
	v_lshlrev_b64 v[38:39], 9, v[38:39]
	v_lshlrev_b64 v[40:41], 9, v[40:41]
	v_lshlrev_b64 v[42:43], 9, v[42:43]
	v_lshlrev_b64 v[44:45], 9, v[44:45]
	v_lshlrev_b64 v[46:47], 9, v[46:47]
	v_lshlrev_b64 v[48:49], 9, v[48:49]
	v_lshlrev_b64 v[50:51], 9, v[50:51]
	v_and_b32_e32 v53, 0x7f, v52
	v_lshl_add_u32 v54, v52, 2, v63
	v_and_b32_e32 v56, 0x7f, v55
	v_lshl_add_u32 v57, v55, 2, v63
	v_and_b32_e32 v59, 0x7f, v58
	v_lshl_add_u32 v60, v58, 2, v63
	v_and_b32_e32 v62, 0x7f, v61
	v_lshl_add_u32 v63, v61, 2, v63
	v_add_u32_e32 v64, v34, v64
	v_lshlrev_b32_e32 v34, 2, v66
	s_mov_b32 s33, s24
	v_readlane_b32 s25, v254, 20
	s_branch .LBB0_117

; #define LAS __attribute__((address_space(3)))
; __device__ __forceinline__ int tid_fresh() { int t = threadIdx.x; asm volatile("" : "+v"(t)); return t; }
; #define CVT_LOAD(jx) do { const int b_ = (jx) / per, r_ = (jx) - b_ * per, kt_ = r_ / tn, nt_ = r_ - kt_ * tn; \
;         const float* s_ = src + (size_t)b_ * sbs + (size_t)(kt_ * 64) * ldS + nt_ * 256; \
;         _Pragma("unroll") for (int q = 0; q < 8; ++q) v[q] = *(const float4*)(s_ + (size_t)(kr + 8 * q) * ldS + c4 * 4); } while (0)
;     const int tid = tid_fresh();
;     const int tk = K / 64, tn = N / 256, per = tk * tn, total = per * nbatch;
;     const int kr = tid >> 6, c4 = tid & 63;
;     ...
;     float4 v[8];
;     if (bid < total) CVT_LOAD(bid);
;     for (int j = bid; j < total; j += G) {
;         const int b = j / per, r = j - b * per, kt = r / tn, ntile = r - kt * tn;
;         __syncthreads();
; #pragma unroll
;         for (int q = 0; q < 8; ++q) { LAS float* tp = tile + (kr + 8 * q) * 257 + c4 * 4; tp[0] = v[q].x; tp[1] = v[q].y; tp[2] = v[q].z; tp[3] = v[q].w; }
;         if (j + G < total) CVT_LOAD(j + G);
;         __syncthreads();
; __global__ void __launch_bounds__(NTHR, 2) fwd(Params p_unused) {
;     ...
;             cvt_group(tile, bid, G, kp->in[30] + (size_t)l * D * FF, 0, FF, D, FF, Wgu + (size_t)NE * 1024 * D, 0, 1, 1, 1024);
;             cvt_group(tile, bid, G, kp->in[31] + (size_t)l * D * FF, 0, FF, D, FF, Wgu + (size_t)NE * 1024 * D, 0, 2, 1, 1024);
.LBB0_117:
	v_add_u32_e32 v65, 0x2020, v64
	s_barrier
	s_waitcnt vmcnt(7)
	ds_write2_b32 v64, v2, v3 offset1:1
	ds_write2_b32 v64, v4, v5 offset0:2 offset1:3
	s_waitcnt vmcnt(6)
	ds_write2_b32 v65, v6, v7 offset1:1
	v_add_u32_e32 v65, 0x2028, v64
	ds_write2_b32 v65, v8, v9 offset1:1
	v_add_u32_e32 v65, 0x4040, v64
	s_waitcnt vmcnt(5)
	ds_write2_b32 v65, v10, v11 offset1:1
	v_add_u32_e32 v65, 0x4048, v64
	ds_write2_b32 v65, v12, v13 offset1:1
	v_add_u32_e32 v65, 0x6060, v64
	s_waitcnt vmcnt(4)
	ds_write2_b32 v65, v14, v15 offset1:1
	v_add_u32_e32 v65, 0x6068, v64
	ds_write2_b32 v65, v16, v17 offset1:1
	v_add_u32_e32 v65, 0x8080, v64
	s_waitcnt vmcnt(3)
	ds_write2_b32 v65, v18, v19 offset1:1
	v_add_u32_e32 v65, 0x8088, v64
	ds_write2_b32 v65, v20, v21 offset1:1
	v_add_u32_e32 v65, 0xa0a0, v64
	s_waitcnt vmcnt(2)
	ds_write2_b32 v65, v22, v23 offset1:1
	v_add_u32_e32 v65, 0xa0a8, v64
	v_readlane_b32 s24, v254, 4
	ds_write2_b32 v65, v24, v25 offset1:1
	v_add_u32_e32 v65, 0xc0c0, v64
	s_add_i32 s31, s33, s24
	s_waitcnt vmcnt(1)
	ds_write2_b32 v65, v26, v27 offset1:1
	v_add_u32_e32 v65, 0xc0c8, v64
	s_cmp_gt_i32 s31, 63
	ds_write2_b32 v65, v28, v29 offset1:1
	v_add_u32_e32 v65, 0xe0e0, v64
	s_cselect_b64 s[24:25], -1, 0
	s_waitcnt vmcnt(0)
	ds_write2_b32 v65, v30, v31 offset1:1
	v_add_u32_e32 v65, 0xe0e8, v64
	s_and_b64 vcc, exec, s[24:25]
	ds_write2_b32 v65, v32, v33 offset1:1
	s_cbranch_vccnz .LBB0_116
	s_ashr_i32 s34, s31, 31
	s_lshr_b32 s34, s34, 26
	s_add_i32 s34, s31, s34
	s_andn2_b32 s34, s34, 63
	s_sub_i32 s36, s31, s34
	s_bfe_u32 s34, s36, 0x10007
	s_add_i32 s34, s36, s34
	s_bfe_i32 s34, s34, 0x80000
	s_sext_i32_i16 s34, s34
	s_ashr_i32 s37, s34, 1
	s_lshl_b32 s34, s37, 6
	s_ashr_i32 s35, s34, 31
	s_lshl_b64 s[34:35], s[34:35], 11
	s_add_u32 s38, s29, s34
	s_addc_u32 s39, s30, s35
	s_lshl_b32 s34, s37, 9
	s_lshl_b32 s35, s36, 8
	s_sub_i32 s34, s35, s34
	s_ashr_i32 s35, s34, 31
	s_lshl_b64 s[34:35], s[34:35], 2
	s_add_u32 s34, s38, s34
	s_addc_u32 s35, s39, s35
	v_lshl_add_u64 v[26:27], s[34:35], 0, v[34:35]
	v_lshl_add_u64 v[10:11], v[36:37], 2, v[26:27]
	v_lshl_add_u64 v[12:13], v[38:39], 2, v[26:27]
	v_lshl_add_u64 v[18:19], v[40:41], 2, v[26:27]
	v_lshl_add_u64 v[20:21], v[42:43], 2, v[26:27]
	v_lshl_add_u64 v[28:29], v[44:45], 2, v[26:27]
	v_lshl_add_u64 v[30:31], v[46:47], 2, v[26:27]
	v_lshl_add_u64 v[66:67], v[48:49], 2, v[26:27]
	global_load_dwordx4 v[2:5], v[10:11], off nt
	global_load_dwordx4 v[6:9], v[12:13], off nt
	s_nop 0
	global_load_dwordx4 v[10:13], v[18:19], off nt
	global_load_dwordx4 v[14:17], v[20:21], off nt
	s_nop 0
	global_load_dwordx4 v[18:21], v[28:29], off nt
	global_load_dwordx4 v[22:25], v[30:31], off nt
	v_lshl_add_u64 v[68:69], v[50:51], 2, v[26:27]
	global_load_dwordx4 v[26:29], v[66:67], off nt
	global_load_dwordx4 v[30:33], v[68:69], off nt
	s_branch .LBB0_116
.LBB0_119:
	v_mov_b32_e32 v58, v0
	s_and_b64 vcc, exec, s[0:1]
	s_barrier
	s_cbranch_vccnz .LBB0_124
	s_load_dwordx2 s[24:25], s[18:19], 0xf8
	s_lshl_b64 s[22:23], s[22:23], 2
	v_and_b32_e32 v1, 63, v58
	v_ashrrev_i32_e32 v52, 6, v58
	v_lshlrev_b32_e32 v34, 4, v1
	s_waitcnt lgkmcnt(0)
	s_add_u32 s24, s24, s22
	s_addc_u32 s25, s25, s23
	s_add_u32 s22, s24, s2
	s_addc_u32 s23, s25, s3
	s_add_u32 s22, s22, s6
	s_addc_u32 s23, s23, s7
	v_ashrrev_i32_e32 v53, 31, v52
	v_add_u32_e32 v38, 8, v52
	s_waitcnt vmcnt(5)
	v_lshl_add_u64 v[26:27], s[22:23], 0, v[34:35]
	v_lshlrev_b64 v[2:3], 11, v[52:53]
	v_ashrrev_i32_e32 v39, 31, v38
	v_add_u32_e32 v40, 16, v52
	v_lshl_add_u64 v[10:11], v[26:27], 0, v[2:3]
	v_lshlrev_b64 v[2:3], 11, v[38:39]
	v_ashrrev_i32_e32 v41, 31, v40
	v_add_u32_e32 v42, 24, v52
	v_lshl_add_u64 v[12:13], v[26:27], 0, v[2:3]
	global_load_dwordx4 v[2:5], v[10:11], off nt
	global_load_dwordx4 v[6:9], v[12:13], off nt
	v_lshlrev_b64 v[10:11], 11, v[40:41]
	v_ashrrev_i32_e32 v43, 31, v42
	v_add_u32_e32 v44, 32, v52
	v_lshl_add_u64 v[18:19], v[26:27], 0, v[10:11]
	v_lshlrev_b64 v[10:11], 11, v[42:43]
	v_ashrrev_i32_e32 v45, 31, v44
	v_add_u32_e32 v46, 40, v52
	v_lshl_add_u64 v[20:21], v[26:27], 0, v[10:11]
	global_load_dwordx4 v[10:13], v[18:19], off nt
	global_load_dwordx4 v[14:17], v[20:21], off nt
	v_lshlrev_b64 v[18:19], 11, v[44:45]
	v_ashrrev_i32_e32 v47, 31, v46
	v_add_u32_e32 v48, 48, v52
	v_lshl_add_u64 v[28:29], v[26:27], 0, v[18:19]
	v_lshlrev_b64 v[18:19], 11, v[46:47]
	v_ashrrev_i32_e32 v49, 31, v48
	v_add_u32_e32 v50, 56, v52
	s_waitcnt vmcnt(8)
	v_lshl_add_u64 v[30:31], v[26:27], 0, v[18:19]
	global_load_dwordx4 v[18:21], v[28:29], off nt
	global_load_dwordx4 v[22:25], v[30:31], off nt
	v_lshlrev_b64 v[28:29], 11, v[48:49]
	v_ashrrev_i32_e32 v51, 31, v50
	v_lshl_add_u64 v[36:37], v[26:27], 0, v[28:29]
	v_lshlrev_b64 v[28:29], 11, v[50:51]
	v_lshl_add_u64 v[54:55], v[26:27], 0, v[28:29]
	global_load_dwordx4 v[26:29], v[36:37], off nt
	global_load_dwordx4 v[30:33], v[54:55], off nt
	v_lshlrev_b32_e32 v66, 2, v1
	v_lshlrev_b64 v[36:37], 9, v[52:53]
	v_and_b32_e32 v1, 7, v58
	v_mul_lo_u32 v64, v52, s17
	v_ashrrev_i32_e32 v52, 3, v58
	v_add_u32_e32 v54, 0x200, v58
	v_add_u32_e32 v56, 0x400, v58
	v_add_u32_e32 v58, 0x600, v58
	v_ashrrev_i32_e32 v54, 3, v54
	v_ashrrev_i32_e32 v56, 3, v56
	v_ashrrev_i32_e32 v58, 3, v58
	v_add_u32_e32 v34, 0, v34
	v_mad_u32_u24 v59, v1, s13, 0
	v_and_b32_e32 v60, 0x7f, v52
	v_and_b32_e32 v61, 0x7f, v54
	v_and_b32_e32 v62, 0x7f, v56
	v_and_b32_e32 v63, 0x7f, v58
	v_readlane_b32 s22, v254, 19
	v_lshlrev_b64 v[38:39], 9, v[38:39]
	v_lshlrev_b64 v[40:41], 9, v[40:41]
	v_lshlrev_b64 v[42:43], 9, v[42:43]
	v_lshlrev_b64 v[44:45], 9, v[44:45]
	v_lshlrev_b64 v[46:47], 9, v[46:47]
	v_lshlrev_b64 v[48:49], 9, v[48:49]
	v_lshlrev_b64 v[50:51], 9, v[50:51]
	v_lshl_add_u32 v53, v52, 2, v59
	v_lshl_add_u32 v55, v54, 2, v59
	v_lshl_add_u32 v57, v56, 2, v59
	v_lshl_add_u32 v59, v58, 2, v59
	v_or_b32_e32 v60, 0x80, v60
	v_or_b32_e32 v61, 0x80, v61
	v_or_b32_e32 v62, 0x80, v62
	v_or_b32_e32 v63, 0x80, v63
	v_add_u32_e32 v64, v34, v64
	v_lshlrev_b32_e32 v34, 2, v66
	s_mov_b32 s30, s22
	v_readlane_b32 s23, v254, 20
	s_branch .LBB0_122

; #define LAS __attribute__((address_space(3)))
; __device__ __forceinline__ int tid_fresh() { int t = threadIdx.x; asm volatile("" : "+v"(t)); return t; }
; #define CVT_LOAD(jx) do { const int b_ = (jx) / per, r_ = (jx) - b_ * per, kt_ = r_ / tn, nt_ = r_ - kt_ * tn; \
;         const float* s_ = src + (size_t)b_ * sbs + (size_t)(kt_ * 64) * ldS + nt_ * 256; \
;         _Pragma("unroll") for (int q = 0; q < 8; ++q) v[q] = *(const float4*)(s_ + (size_t)(kr + 8 * q) * ldS + c4 * 4); } while (0)
;     const int tid = tid_fresh();
;     const int tk = K / 64, tn = N / 256, per = tk * tn, total = per * nbatch;
;     const int kr = tid >> 6, c4 = tid & 63;
;     ...
;     float4 v[8];
;     if (bid < total) CVT_LOAD(bid);
;     for (int j = bid; j < total; j += G) {
;         const int b = j / per, r = j - b * per, kt = r / tn, ntile = r - kt * tn;
;         __syncthreads();
; #pragma unroll
;         for (int q = 0; q < 8; ++q) { LAS float* tp = tile + (kr + 8 * q) * 257 + c4 * 4; tp[0] = v[q].x; tp[1] = v[q].y; tp[2] = v[q].z; tp[3] = v[q].w; }
;         if (j + G < total) CVT_LOAD(j + G);
;         __syncthreads();
; __global__ void __launch_bounds__(NTHR, 2) fwd(Params p_unused) {
;     ...
;             cvt_group(tile, bid, G, kp->in[32] + (size_t)l * FF * D, 0, D, FF, D, Wd + (size_t)NE * D * FF, 0, 0, 1, D);
.LBB0_122:
	v_add_u32_e32 v65, 0x2020, v64
	s_barrier
	s_waitcnt vmcnt(7)
	ds_write2_b32 v64, v2, v3 offset1:1
	ds_write2_b32 v64, v4, v5 offset0:2 offset1:3
	s_waitcnt vmcnt(6)
	ds_write2_b32 v65, v6, v7 offset1:1
	v_add_u32_e32 v65, 0x2028, v64
	ds_write2_b32 v65, v8, v9 offset1:1
	v_add_u32_e32 v65, 0x4040, v64
	s_waitcnt vmcnt(5)
	ds_write2_b32 v65, v10, v11 offset1:1
	v_add_u32_e32 v65, 0x4048, v64
	ds_write2_b32 v65, v12, v13 offset1:1
	v_add_u32_e32 v65, 0x6060, v64
	s_waitcnt vmcnt(4)
	ds_write2_b32 v65, v14, v15 offset1:1
	v_add_u32_e32 v65, 0x6068, v64
	ds_write2_b32 v65, v16, v17 offset1:1
	v_add_u32_e32 v65, 0x8080, v64
	s_waitcnt vmcnt(3)
	ds_write2_b32 v65, v18, v19 offset1:1
	v_add_u32_e32 v65, 0x8088, v64
	ds_write2_b32 v65, v20, v21 offset1:1
	v_add_u32_e32 v65, 0xa0a0, v64
	s_waitcnt vmcnt(2)
	ds_write2_b32 v65, v22, v23 offset1:1
	v_add_u32_e32 v65, 0xa0a8, v64
	v_readlane_b32 s22, v254, 4
	ds_write2_b32 v65, v24, v25 offset1:1
	v_add_u32_e32 v65, 0xc0c0, v64
	s_add_i32 s29, s30, s22
	s_waitcnt vmcnt(1)
	ds_write2_b32 v65, v26, v27 offset1:1
	v_add_u32_e32 v65, 0xc0c8, v64
	s_cmp_gt_i32 s29, 63
	ds_write2_b32 v65, v28, v29 offset1:1
	v_add_u32_e32 v65, 0xe0e0, v64
	s_cselect_b64 s[22:23], -1, 0
	s_waitcnt vmcnt(0)
	ds_write2_b32 v65, v30, v31 offset1:1
	v_add_u32_e32 v65, 0xe0e8, v64
	s_and_b64 vcc, exec, s[22:23]
	ds_write2_b32 v65, v32, v33 offset1:1
	s_cbranch_vccnz .LBB0_121
	s_ashr_i32 s31, s29, 31
	s_lshr_b32 s31, s31, 26
	s_add_i32 s31, s29, s31
	s_andn2_b32 s31, s31, 63
	s_sub_i32 s31, s29, s31
	s_bfe_u32 s33, s31, 0x10007
	s_add_i32 s33, s31, s33
	s_bfe_i32 s33, s33, 0x80000
	s_sext_i32_i16 s33, s33
	s_ashr_i32 s33, s33, 1
	s_lshl_b32 s34, s33, 6
	s_ashr_i32 s35, s34, 31
	s_lshl_b64 s[34:35], s[34:35], 11
	s_add_u32 s36, s24, s34
	s_addc_u32 s37, s25, s35
	s_lshl_b32 s33, s33, 9
	s_lshl_b32 s31, s31, 8
	s_sub_i32 s34, s31, s33
	s_ashr_i32 s35, s34, 31
	s_lshl_b64 s[34:35], s[34:35], 2
	s_add_u32 s34, s36, s34
	s_addc_u32 s35, s37, s35
	v_lshl_add_u64 v[26:27], s[34:35], 0, v[34:35]
	v_lshl_add_u64 v[10:11], v[36:37], 2, v[26:27]
	v_lshl_add_u64 v[12:13], v[38:39], 2, v[26:27]
	v_lshl_add_u64 v[18:19], v[40:41], 2, v[26:27]
	v_lshl_add_u64 v[20:21], v[42:43], 2, v[26:27]
	v_lshl_add_u64 v[28:29], v[44:45], 2, v[26:27]
	v_lshl_add_u64 v[30:31], v[46:47], 2, v[26:27]
	v_lshl_add_u64 v[66:67], v[48:49], 2, v[26:27]
	global_load_dwordx4 v[2:5], v[10:11], off nt
	global_load_dwordx4 v[6:9], v[12:13], off nt
	s_nop 0
	global_load_dwordx4 v[10:13], v[18:19], off nt
	global_load_dwordx4 v[14:17], v[20:21], off nt
	s_nop 0
	global_load_dwordx4 v[18:21], v[28:29], off nt
	global_load_dwordx4 v[22:25], v[30:31], off nt
	v_lshl_add_u64 v[68:69], v[50:51], 2, v[26:27]
	global_load_dwordx4 v[26:29], v[66:67], off nt
	global_load_dwordx4 v[30:33], v[68:69], off nt
	s_branch .LBB0_121
.LBB0_124:
	v_mov_b32_e32 v58, v0
	s_and_b64 vcc, exec, s[0:1]
	s_barrier
	s_cbranch_vccnz .LBB0_113
	s_mul_hi_u32 s21, s14, 0xf7e00000
	s_load_dwordx2 s[18:19], s[18:19], 0x100
	s_mul_i32 s20, s15, 0xf7e00000
	s_sub_i32 s21, s21, s14
	s_add_i32 s21, s21, s20
	s_mul_i32 s20, s14, 0xf7e00000
	s_add_u32 s22, s27, s20
	s_addc_u32 s23, s28, s21
	s_lshl_b64 s[14:15], s[14:15], 22
	s_waitcnt lgkmcnt(0)
	s_add_u32 s20, s18, s14
	s_addc_u32 s21, s19, s15
	s_add_u32 s14, s22, 0x2c830000
	s_addc_u32 s15, s23, 0
	s_add_u32 s18, s20, s4
	s_addc_u32 s19, s21, s5
	v_and_b32_e32 v1, 63, v58
	v_ashrrev_i32_e32 v52, 6, v58
	s_add_u32 s18, s18, s10
	s_addc_u32 s19, s19, s11
	v_lshlrev_b32_e32 v34, 4, v1
	v_ashrrev_i32_e32 v53, 31, v52
	v_add_u32_e32 v38, 8, v52
	s_waitcnt vmcnt(5)
	v_lshl_add_u64 v[26:27], s[18:19], 0, v[34:35]
	v_lshlrev_b64 v[2:3], 13, v[52:53]
	v_ashrrev_i32_e32 v39, 31, v38
	v_add_u32_e32 v40, 16, v52
	v_lshl_add_u64 v[10:11], v[26:27], 0, v[2:3]
	v_lshlrev_b64 v[2:3], 13, v[38:39]
	v_ashrrev_i32_e32 v41, 31, v40
	v_add_u32_e32 v42, 24, v52
	v_lshl_add_u64 v[12:13], v[26:27], 0, v[2:3]
	global_load_dwordx4 v[2:5], v[10:11], off nt
	global_load_dwordx4 v[6:9], v[12:13], off nt
	v_lshlrev_b64 v[10:11], 13, v[40:41]
	v_ashrrev_i32_e32 v43, 31, v42
	v_add_u32_e32 v44, 32, v52
	v_lshl_add_u64 v[18:19], v[26:27], 0, v[10:11]
	v_lshlrev_b64 v[10:11], 13, v[42:43]
	v_ashrrev_i32_e32 v45, 31, v44
	v_add_u32_e32 v46, 40, v52
	v_lshl_add_u64 v[20:21], v[26:27], 0, v[10:11]
	global_load_dwordx4 v[10:13], v[18:19], off nt
	global_load_dwordx4 v[14:17], v[20:21], off nt
	v_lshlrev_b64 v[18:19], 13, v[44:45]
	v_ashrrev_i32_e32 v47, 31, v46
	v_add_u32_e32 v48, 48, v52
	v_lshl_add_u64 v[28:29], v[26:27], 0, v[18:19]
	v_lshlrev_b64 v[18:19], 13, v[46:47]
	v_ashrrev_i32_e32 v49, 31, v48
	v_add_u32_e32 v50, 56, v52
	s_waitcnt vmcnt(8)
	v_lshl_add_u64 v[30:31], v[26:27], 0, v[18:19]
	global_load_dwordx4 v[18:21], v[28:29], off nt
	global_load_dwordx4 v[22:25], v[30:31], off nt
	v_lshlrev_b64 v[28:29], 13, v[48:49]
	v_ashrrev_i32_e32 v51, 31, v50
	v_lshl_add_u64 v[36:37], v[26:27], 0, v[28:29]
	v_lshlrev_b64 v[28:29], 13, v[50:51]
	v_lshl_add_u64 v[54:55], v[26:27], 0, v[28:29]
	global_load_dwordx4 v[26:29], v[36:37], off nt
	global_load_dwordx4 v[30:33], v[54:55], off nt
	v_lshlrev_b32_e32 v62, 2, v1
	v_lshlrev_b64 v[36:37], 11, v[52:53]
	v_and_b32_e32 v1, 7, v58
	v_mul_lo_u32 v60, v52, s17
	v_ashrrev_i32_e32 v52, 3, v58
	v_add_u32_e32 v54, 0x200, v58
	v_add_u32_e32 v56, 0x400, v58
	v_add_u32_e32 v58, 0x600, v58
	v_add_u32_e32 v34, 0, v34
	v_mad_u32_u24 v59, v1, s13, 0
	v_ashrrev_i32_e32 v54, 3, v54
	v_ashrrev_i32_e32 v56, 3, v56
	v_ashrrev_i32_e32 v58, 3, v58
	v_readlane_b32 s18, v254, 19
	v_lshlrev_b64 v[38:39], 11, v[38:39]
	v_lshlrev_b64 v[40:41], 11, v[40:41]
	v_lshlrev_b64 v[42:43], 11, v[42:43]
	v_lshlrev_b64 v[44:45], 11, v[44:45]
	v_lshlrev_b64 v[46:47], 11, v[46:47]
	v_lshlrev_b64 v[48:49], 11, v[48:49]
	v_lshlrev_b64 v[50:51], 11, v[50:51]
	v_lshl_add_u32 v53, v52, 2, v59
	v_lshl_add_u32 v55, v54, 2, v59
	v_lshl_add_u32 v57, v56, 2, v59
	v_lshl_add_u32 v59, v58, 2, v59
	v_add_u32_e32 v60, v34, v60
	v_lshlrev_b32_e32 v34, 2, v62
	s_mov_b32 s23, s18
	v_readlane_b32 s19, v254, 20
	s_branch .LBB0_127

; #define LAS __attribute__((address_space(3)))
; #define CVT_LOAD(jx) do { const int b_ = (jx) / per, r_ = (jx) - b_ * per, kt_ = r_ / tn, nt_ = r_ - kt_ * tn; \
;         const float* s_ = src + (size_t)b_ * sbs + (size_t)(kt_ * 64) * ldS + nt_ * 256; \
;         _Pragma("unroll") for (int q = 0; q < 8; ++q) v[q] = *(const float4*)(s_ + (size_t)(kr + 8 * q) * ldS + c4 * 4); } while (0)
;     ...
;     for (int j = bid; j < total; j += G) {
;         const int b = j / per, r = j - b * per, kt = r / tn, ntile = r - kt * tn;
;         __syncthreads();
; #pragma unroll
;         for (int q = 0; q < 8; ++q) { LAS float* tp = tile + (kr + 8 * q) * 257 + c4 * 4; tp[0] = v[q].x; tp[1] = v[q].y; tp[2] = v[q].z; tp[3] = v[q].w; }
;         if (j + G < total) CVT_LOAD(j + G);
;         __syncthreads();
.LBB0_127:
	v_add_u32_e32 v61, 0x2020, v60
	s_barrier
	s_waitcnt vmcnt(7)
	ds_write2_b32 v60, v2, v3 offset1:1
	ds_write2_b32 v60, v4, v5 offset0:2 offset1:3
	s_waitcnt vmcnt(6)
	ds_write2_b32 v61, v6, v7 offset1:1
	v_add_u32_e32 v61, 0x2028, v60
	ds_write2_b32 v61, v8, v9 offset1:1
	v_add_u32_e32 v61, 0x4040, v60
	s_waitcnt vmcnt(5)
	ds_write2_b32 v61, v10, v11 offset1:1
	v_add_u32_e32 v61, 0x4048, v60
	ds_write2_b32 v61, v12, v13 offset1:1
	v_add_u32_e32 v61, 0x6060, v60
	s_waitcnt vmcnt(4)
	ds_write2_b32 v61, v14, v15 offset1:1
	v_add_u32_e32 v61, 0x6068, v60
	ds_write2_b32 v61, v16, v17 offset1:1
	v_add_u32_e32 v61, 0x8080, v60
	s_waitcnt vmcnt(3)
	ds_write2_b32 v61, v18, v19 offset1:1
	v_add_u32_e32 v61, 0x8088, v60
	ds_write2_b32 v61, v20, v21 offset1:1
	v_add_u32_e32 v61, 0xa0a0, v60
	s_waitcnt vmcnt(2)
	ds_write2_b32 v61, v22, v23 offset1:1
	v_add_u32_e32 v61, 0xa0a8, v60
	v_readlane_b32 s18, v254, 4
	ds_write2_b32 v61, v24, v25 offset1:1
	v_add_u32_e32 v61, 0xc0c0, v60
	s_add_i32 s22, s23, s18
	s_waitcnt vmcnt(1)
	ds_write2_b32 v61, v26, v27 offset1:1
	v_add_u32_e32 v61, 0xc0c8, v60
	s_cmp_gt_i32 s22, 63
	ds_write2_b32 v61, v28, v29 offset1:1
	v_add_u32_e32 v61, 0xe0e0, v60
	s_cselect_b64 s[18:19], -1, 0
	s_waitcnt vmcnt(0)
	ds_write2_b32 v61, v30, v31 offset1:1
	v_add_u32_e32 v61, 0xe0e8, v60
	s_and_b64 vcc, exec, s[18:19]
	ds_write2_b32 v61, v32, v33 offset1:1
	s_cbranch_vccnz .LBB0_126
	s_ashr_i32 s24, s22, 31
	s_lshr_b32 s24, s24, 26
	s_add_i32 s24, s22, s24
	s_andn2_b32 s24, s24, 63
	s_sub_i32 s27, s22, s24
	s_bfe_i32 s24, s27, 0x80000
	s_bfe_u32 s24, s24, 0x3000c
	s_add_i32 s24, s27, s24
	s_bfe_i32 s24, s24, 0x80000
	s_sext_i32_i16 s24, s24
	s_ashr_i32 s28, s24, 3
	s_lshl_b32 s24, s28, 6
	s_ashr_i32 s25, s24, 31
	s_lshl_b64 s[24:25], s[24:25], 13
	s_add_u32 s29, s20, s24
	s_addc_u32 s30, s21, s25
	s_lshl_b32 s24, s28, 11
	s_lshl_b32 s25, s27, 8
	s_sub_i32 s24, s25, s24
	s_ashr_i32 s25, s24, 31
	s_lshl_b64 s[24:25], s[24:25], 2
	s_add_u32 s24, s29, s24
	s_addc_u32 s25, s30, s25
	v_lshl_add_u64 v[26:27], s[24:25], 0, v[34:35]
	v_lshl_add_u64 v[10:11], v[36:37], 2, v[26:27]
	v_lshl_add_u64 v[12:13], v[38:39], 2, v[26:27]
	v_lshl_add_u64 v[18:19], v[40:41], 2, v[26:27]
	v_lshl_add_u64 v[20:21], v[42:43], 2, v[26:27]
	v_lshl_add_u64 v[28:29], v[44:45], 2, v[26:27]
	v_lshl_add_u64 v[30:31], v[46:47], 2, v[26:27]
	v_lshl_add_u64 v[62:63], v[48:49], 2, v[26:27]
	global_load_dwordx4 v[2:5], v[10:11], off nt
	global_load_dwordx4 v[6:9], v[12:13], off nt
	s_nop 0
	global_load_dwordx4 v[10:13], v[18:19], off nt
	global_load_dwordx4 v[14:17], v[20:21], off nt
	s_nop 0
	global_load_dwordx4 v[18:21], v[28:29], off nt
	global_load_dwordx4 v[22:25], v[30:31], off nt
	v_lshl_add_u64 v[64:65], v[50:51], 2, v[26:27]
	global_load_dwordx4 v[26:29], v[62:63], off nt
	global_load_dwordx4 v[30:33], v[64:65], off nt
	s_branch .LBB0_126
